# expert GEMM epilogues: leading half (wr=0) runs its epilogue at priority 1 so its next-unit load segment overlaps the trailing half's epilogue
# baseline (speedup 1.0000x reference)
.LBB0_1916:
	s_cmp_lg_u64 s[16:17], 0
	s_cbranch_scc0 .Lepi6_noprio
	s_setprio 1
.Lepi6_noprio:
	s_mov_b32 s29, 0
	v_mov_b32_e32 v4, v166
	v_mov_b32_e32 v2, v167
	v_mov_b32_e32 v3, s24
	s_add_u32 s40, s2, 0xffffff00
	ds_read_b32 v3, v3 offset:288
	s_addc_u32 s41, s23, -1
	s_lshl_b32 s2, s31, 11
	s_add_i32 s2, s2, 0
	v_lshl_add_u32 v18, v2, 3, s83
	s_add_i32 s2, s2, 0x21000
	v_lshl_add_u32 v5, v18, 3, s2
	ds_read_b128 v[14:17], v5
	s_waitcnt lgkmcnt(1)
	v_readfirstlane_b32 s8, v3
	s_lshl_b32 s8, s8, 2
	s_add_i32 s8, s8, 0
	s_add_i32 s8, s8, 0x201c0
	v_mov_b32_e32 v2, s8
	ds_read2_b32 v[2:3], v2 offset1:32
	v_add_u32_e32 v19, s82, v4
	ds_read_b128 v[10:13], v5 offset:16
	ds_read_b128 v[6:9], v5 offset:32
	v_add_u32_e32 v22, 16, v19
	v_add_u32_e32 v24, 32, v19
	s_waitcnt lgkmcnt(2)
	v_readfirstlane_b32 s9, v2
	v_lshl_add_u32 v2, v19, 2, s2
	ds_read_b32 v20, v2 offset:1024
	v_readfirstlane_b32 s8, v3
	s_sub_i32 s8, s36, s8
	v_lshl_add_u32 v23, v22, 2, s2
	v_lshl_add_u32 v25, v24, 2, s2
	s_lshl_b32 s8, s8, 8
	ds_read_b128 v[2:5], v5 offset:48
	ds_read_b32 v23, v23 offset:1024
	ds_read_b32 v25, v25 offset:1024
	v_add_u32_e32 v21, s8, v19
	s_waitcnt lgkmcnt(3)
	v_mul_f32_e32 v20, 0x3b800000, v20
	v_cmp_gt_i32_e32 vcc, s9, v21
	s_waitcnt lgkmcnt(1)
	v_mul_f32_e32 v21, 0x3b800000, v23
	v_add_u32_e32 v26, 0xa0, v19
	v_cndmask_b32_e32 v180, 0, v20, vcc
	v_add_u32_e32 v20, s8, v22
	v_cmp_gt_i32_e32 vcc, s9, v20
	v_add_u32_e32 v20, s8, v24
	v_add_u32_e32 v22, 0x80, v19
	v_cndmask_b32_e32 v164, 0, v21, vcc
	s_waitcnt lgkmcnt(0)
	v_mul_f32_e32 v21, 0x3b800000, v25
	v_cmp_gt_i32_e32 vcc, s9, v20
	v_add_u32_e32 v20, 48, v19
	v_add_u32_e32 v24, 0x90, v19
	v_cndmask_b32_e32 v162, 0, v21, vcc
	v_lshl_add_u32 v21, v20, 2, s2
	v_lshl_add_u32 v23, v22, 2, s2
	v_lshl_add_u32 v25, v24, 2, s2
	v_lshl_add_u32 v27, v26, 2, s2
	v_add_u32_e32 v29, 0xb0, v19
	v_add_u32_e32 v20, s8, v20
	v_lshl_add_u32 v28, v29, 2, s2
	ds_read_b32 v21, v21 offset:1024
	ds_read_b32 v23, v23 offset:1024
	ds_read_b32 v25, v25 offset:1024
	ds_read_b32 v27, v27 offset:1024
	ds_read_b32 v31, v28 offset:1024
	s_waitcnt lgkmcnt(4)
	v_mul_f32_e32 v21, 0x3b800000, v21
	v_cmp_gt_i32_e32 vcc, s9, v20
	v_add_u32_e32 v20, s8, v22
	s_lshl_b32 s42, s14, 7
	v_cndmask_b32_e32 v32, 0, v21, vcc
	s_waitcnt lgkmcnt(3)
	v_mul_f32_e32 v21, 0x3b800000, v23
	v_cmp_gt_i32_e32 vcc, s9, v20
	v_add_u32_e32 v20, s8, v24
	v_mov_b32_e32 v24, v14
	v_cndmask_b32_e32 v30, 0, v21, vcc
	s_waitcnt lgkmcnt(2)
	v_mul_f32_e32 v21, 0x3b800000, v25
	v_mov_b32_e32 v25, v16
	v_pk_fma_f32 v[182:183], v[158:159], v[180:181], v[24:25] op_sel_hi:[1,0,1]
	v_mov_b32_e32 v16, v15
	v_min_f32_e32 v182, 0x40e00000, v182
	v_min_f32_e32 v183, 0x40e00000, v183
	v_pk_mul_f32 v[184:185], v[182:183], s[20:21] op_sel_hi:[1,0]
	v_cmp_gt_i32_e32 vcc, s9, v20
	v_exp_f32_e32 v184, v184
	v_exp_f32_e32 v185, v185
	v_add_u32_e32 v20, s8, v26
	v_cndmask_b32_e32 v28, 0, v21, vcc
	s_waitcnt lgkmcnt(1)
	v_mul_f32_e32 v21, 0x3b800000, v27
	v_pk_add_f32 v[14:15], v[184:185], 1.0 op_sel_hi:[1,0]
	v_pk_fma_f32 v[184:185], v[126:127], v[180:181], v[16:17] op_sel_hi:[1,0,1]
	v_rcp_f32_e32 v14, v14
	v_rcp_f32_e32 v15, v15
	v_med3_f32 v184, v184, s37, v176
	v_med3_f32 v185, v185, s37, v176
	v_cmp_gt_i32_e32 vcc, s9, v20
	v_pk_mul_f32 v[14:15], v[182:183], v[14:15]
	v_add_u32_e32 v20, s8, v29
	v_pk_fma_f32 v[182:183], v[184:185], v[14:15], v[14:15]
	v_mov_b32_e32 v14, v10
	v_mov_b32_e32 v15, v12
	v_pk_fma_f32 v[184:185], v[160:161], v[180:181], v[14:15] op_sel_hi:[1,0,1]
	v_mov_b32_e32 v12, v11
	v_min_f32_e32 v184, 0x40e00000, v184
	v_min_f32_e32 v185, 0x40e00000, v185
	v_pk_mul_f32 v[186:187], v[184:185], s[20:21] op_sel_hi:[1,0]
	v_cndmask_b32_e32 v26, 0, v21, vcc
	v_exp_f32_e32 v186, v186
	v_exp_f32_e32 v187, v187
	s_waitcnt lgkmcnt(0)
	v_mul_f32_e32 v21, 0x3b800000, v31
	v_cmp_gt_i32_e32 vcc, s9, v20
	v_pk_add_f32 v[10:11], v[186:187], 1.0 op_sel_hi:[1,0]
	v_cndmask_b32_e32 v22, 0, v21, vcc
	v_rcp_f32_e32 v10, v10
	v_rcp_f32_e32 v11, v11
	v_cvt_pk_fp8_f32 v192, v182, v183
	v_pk_fma_f32 v[182:183], v[128:129], v[180:181], v[12:13] op_sel_hi:[1,0,1]
	v_pk_mul_f32 v[10:11], v[184:185], v[10:11]
	v_med3_f32 v182, v182, s37, v176
	v_med3_f32 v183, v183, s37, v176
	v_pk_fma_f32 v[182:183], v[182:183], v[10:11], v[10:11]
	v_mov_b32_e32 v10, v6
	v_mov_b32_e32 v11, v8
	v_pk_fma_f32 v[184:185], v[154:155], v[180:181], v[10:11] op_sel_hi:[1,0,1]
	v_mov_b32_e32 v8, v7
	v_min_f32_e32 v184, 0x40e00000, v184
	v_min_f32_e32 v185, 0x40e00000, v185
	v_pk_mul_f32 v[186:187], v[184:185], s[20:21] op_sel_hi:[1,0]
	v_cvt_pk_fp8_f32 v192, v182, v183 op_sel:[0,0,1]
	v_exp_f32_e32 v186, v186
	v_exp_f32_e32 v187, v187
	v_pk_fma_f32 v[182:183], v[122:123], v[180:181], v[8:9] op_sel_hi:[1,0,1]
	v_med3_f32 v182, v182, s37, v176
	v_pk_add_f32 v[6:7], v[186:187], 1.0 op_sel_hi:[1,0]
	v_med3_f32 v183, v183, s37, v176
	v_rcp_f32_e32 v6, v6
	v_rcp_f32_e32 v7, v7
	v_lshl_add_u32 v20, s36, 8, v19
	s_ashr_i32 s43, s42, 31
	v_pk_mul_f32 v[6:7], v[184:185], v[6:7]
	v_ashrrev_i32_e32 v19, 31, v18
	v_pk_fma_f32 v[182:183], v[182:183], v[6:7], v[6:7]
	v_mov_b32_e32 v6, v2
	v_mov_b32_e32 v7, v4
	v_pk_fma_f32 v[184:185], v[156:157], v[180:181], v[6:7] op_sel_hi:[1,0,1]
	v_mov_b32_e32 v4, v3
	v_min_f32_e32 v184, 0x40e00000, v184
	v_min_f32_e32 v185, 0x40e00000, v185
	v_pk_mul_f32 v[186:187], v[184:185], s[20:21] op_sel_hi:[1,0]
	v_pk_fma_f32 v[180:181], v[124:125], v[180:181], v[4:5] op_sel_hi:[1,0,1]
	v_exp_f32_e32 v186, v186
	v_exp_f32_e32 v187, v187
	v_cvt_pk_fp8_f32 v193, v182, v183
	v_med3_f32 v180, v180, s37, v176
	v_med3_f32 v181, v181, s37, v176
	v_pk_add_f32 v[2:3], v[186:187], 1.0 op_sel_hi:[1,0]
	v_pk_fma_f32 v[182:183], v[150:151], v[164:165], v[24:25] op_sel_hi:[1,0,1]
	v_rcp_f32_e32 v2, v2
	v_rcp_f32_e32 v3, v3
	v_min_f32_e32 v182, 0x40e00000, v182
	v_min_f32_e32 v183, 0x40e00000, v183
	s_and_b64 vcc, exec, s[6:7]
	v_pk_mul_f32 v[2:3], v[184:185], v[2:3]
	v_pk_mul_f32 v[184:185], v[182:183], s[20:21] op_sel_hi:[1,0]
	v_pk_fma_f32 v[2:3], v[180:181], v[2:3], v[2:3]
	v_exp_f32_e32 v184, v184
	v_cvt_pk_fp8_f32 v193, v2, v3 op_sel:[0,0,1]
	v_ashrrev_i32_e32 v21, 31, v20
	v_lshlrev_b64 v[180:181], 10, v[20:21]
	v_exp_f32_e32 v185, v185
	v_lshl_add_u64 v[180:181], s[12:13], 0, v[180:181]
	v_lshl_add_u64 v[180:181], v[180:181], 0, s[42:43]
	v_lshl_add_u64 v[188:189], v[180:181], 0, v[18:19]
	global_store_dwordx2 v[188:189], v[192:193], off
	v_pk_add_f32 v[2:3], v[184:185], 1.0 op_sel_hi:[1,0]
	v_pk_fma_f32 v[180:181], v[118:119], v[164:165], v[16:17] op_sel_hi:[1,0,1]
	v_rcp_f32_e32 v2, v2
	v_rcp_f32_e32 v3, v3
	v_med3_f32 v180, v180, s37, v176
	v_med3_f32 v181, v181, s37, v176
	v_pk_mul_f32 v[2:3], v[182:183], v[2:3]
	v_pk_fma_f32 v[182:183], v[152:153], v[164:165], v[14:15] op_sel_hi:[1,0,1]
	v_pk_fma_f32 v[2:3], v[180:181], v[2:3], v[2:3]
	v_min_f32_e32 v182, 0x40e00000, v182
	v_min_f32_e32 v183, 0x40e00000, v183
	v_pk_mul_f32 v[184:185], v[182:183], s[20:21] op_sel_hi:[1,0]
	v_cvt_pk_fp8_f32 v194, v2, v3
	v_exp_f32_e32 v184, v184
	v_exp_f32_e32 v185, v185
	v_pk_fma_f32 v[180:181], v[120:121], v[164:165], v[12:13] op_sel_hi:[1,0,1]
	v_med3_f32 v180, v180, s37, v176
	v_pk_add_f32 v[2:3], v[184:185], 1.0 op_sel_hi:[1,0]
	v_med3_f32 v181, v181, s37, v176
	v_rcp_f32_e32 v2, v2
	v_rcp_f32_e32 v3, v3
	s_nop 0
	v_pk_mul_f32 v[2:3], v[182:183], v[2:3]
	v_pk_fma_f32 v[182:183], v[146:147], v[164:165], v[10:11] op_sel_hi:[1,0,1]
	v_pk_fma_f32 v[2:3], v[180:181], v[2:3], v[2:3]
	v_min_f32_e32 v182, 0x40e00000, v182
	v_min_f32_e32 v183, 0x40e00000, v183
	v_pk_mul_f32 v[184:185], v[182:183], s[20:21] op_sel_hi:[1,0]
	v_cvt_pk_fp8_f32 v194, v2, v3 op_sel:[0,0,1]
	v_exp_f32_e32 v184, v184
	v_exp_f32_e32 v185, v185
	v_pk_fma_f32 v[180:181], v[114:115], v[164:165], v[8:9] op_sel_hi:[1,0,1]
	v_pk_add_f32 v[2:3], v[184:185], 1.0 op_sel_hi:[1,0]
	s_nop 0
	v_rcp_f32_e32 v2, v2
	v_rcp_f32_e32 v3, v3
	v_med3_f32 v180, v180, s37, v176
	v_med3_f32 v181, v181, s37, v176
	v_pk_mul_f32 v[2:3], v[182:183], v[2:3]
	v_pk_fma_f32 v[182:183], v[148:149], v[164:165], v[6:7] op_sel_hi:[1,0,1]
	v_pk_fma_f32 v[2:3], v[180:181], v[2:3], v[2:3]
	v_min_f32_e32 v182, 0x40e00000, v182
	v_min_f32_e32 v183, 0x40e00000, v183
	v_pk_mul_f32 v[184:185], v[182:183], s[20:21] op_sel_hi:[1,0]
	v_cvt_pk_fp8_f32 v195, v2, v3
	v_exp_f32_e32 v184, v184
	v_exp_f32_e32 v185, v185
	v_pk_fma_f32 v[180:181], v[116:117], v[164:165], v[4:5] op_sel_hi:[1,0,1]
	v_pk_add_f32 v[2:3], v[184:185], 1.0 op_sel_hi:[1,0]
	s_nop 0
	v_rcp_f32_e32 v2, v2
	v_rcp_f32_e32 v3, v3
	v_med3_f32 v180, v180, s37, v176
	v_med3_f32 v181, v181, s37, v176
	v_pk_mul_f32 v[2:3], v[182:183], v[2:3]
	v_pk_fma_f32 v[182:183], v[142:143], v[162:163], v[24:25] op_sel_hi:[1,0,1]
	v_pk_fma_f32 v[2:3], v[180:181], v[2:3], v[2:3]
	v_min_f32_e32 v182, 0x40e00000, v182
	v_min_f32_e32 v183, 0x40e00000, v183
	v_cvt_pk_fp8_f32 v195, v2, v3 op_sel:[0,0,1]
	v_pk_mul_f32 v[184:185], v[182:183], s[20:21] op_sel_hi:[1,0]
	v_exp_f32_e32 v184, v184
	v_exp_f32_e32 v185, v185
	s_mov_b32 s28, 0x4000
	v_lshl_add_u64 v[180:181], v[188:189], 0, s[28:29]
	global_store_dwordx2 v[180:181], v[194:195], off
	v_pk_add_f32 v[2:3], v[184:185], 1.0 op_sel_hi:[1,0]
	v_pk_fma_f32 v[180:181], v[110:111], v[162:163], v[16:17] op_sel_hi:[1,0,1]
	v_rcp_f32_e32 v2, v2
	v_rcp_f32_e32 v3, v3
	v_med3_f32 v180, v180, s37, v176
	v_med3_f32 v181, v181, s37, v176
	v_pk_mul_f32 v[2:3], v[182:183], v[2:3]
	v_pk_fma_f32 v[182:183], v[144:145], v[162:163], v[14:15] op_sel_hi:[1,0,1]
	v_pk_fma_f32 v[2:3], v[180:181], v[2:3], v[2:3]
	v_min_f32_e32 v182, 0x40e00000, v182
	v_min_f32_e32 v183, 0x40e00000, v183
	v_pk_mul_f32 v[184:185], v[182:183], s[20:21] op_sel_hi:[1,0]
	v_cvt_pk_fp8_f32 v196, v2, v3
	v_exp_f32_e32 v184, v184
	v_exp_f32_e32 v185, v185
	v_pk_fma_f32 v[180:181], v[112:113], v[162:163], v[12:13] op_sel_hi:[1,0,1]
	v_med3_f32 v180, v180, s37, v176
	v_pk_add_f32 v[2:3], v[184:185], 1.0 op_sel_hi:[1,0]
	v_med3_f32 v181, v181, s37, v176
	v_rcp_f32_e32 v2, v2
	v_rcp_f32_e32 v3, v3
	s_nop 0
	v_pk_mul_f32 v[2:3], v[182:183], v[2:3]
	v_pk_fma_f32 v[182:183], v[138:139], v[162:163], v[10:11] op_sel_hi:[1,0,1]
	v_pk_fma_f32 v[2:3], v[180:181], v[2:3], v[2:3]
	v_min_f32_e32 v182, 0x40e00000, v182
	v_min_f32_e32 v183, 0x40e00000, v183
	v_pk_mul_f32 v[184:185], v[182:183], s[20:21] op_sel_hi:[1,0]
	v_cvt_pk_fp8_f32 v196, v2, v3 op_sel:[0,0,1]
	v_exp_f32_e32 v184, v184
	v_exp_f32_e32 v185, v185
	v_pk_fma_f32 v[180:181], v[106:107], v[162:163], v[8:9] op_sel_hi:[1,0,1]
	v_pk_add_f32 v[2:3], v[184:185], 1.0 op_sel_hi:[1,0]
	s_nop 0
	v_rcp_f32_e32 v2, v2
	v_rcp_f32_e32 v3, v3
	v_med3_f32 v180, v180, s37, v176
	v_med3_f32 v181, v181, s37, v176
	v_pk_mul_f32 v[2:3], v[182:183], v[2:3]
	v_pk_fma_f32 v[182:183], v[140:141], v[162:163], v[6:7] op_sel_hi:[1,0,1]
	v_pk_fma_f32 v[2:3], v[180:181], v[2:3], v[2:3]
	v_min_f32_e32 v182, 0x40e00000, v182
	v_min_f32_e32 v183, 0x40e00000, v183
	v_pk_mul_f32 v[184:185], v[182:183], s[20:21] op_sel_hi:[1,0]
	v_cvt_pk_fp8_f32 v197, v2, v3
	v_exp_f32_e32 v184, v184
	v_exp_f32_e32 v185, v185
	v_pk_fma_f32 v[180:181], v[108:109], v[162:163], v[4:5] op_sel_hi:[1,0,1]
	v_pk_add_f32 v[2:3], v[184:185], 1.0 op_sel_hi:[1,0]
	s_nop 0
	v_rcp_f32_e32 v2, v2
	v_rcp_f32_e32 v3, v3
	v_med3_f32 v180, v180, s37, v176
	v_med3_f32 v181, v181, s37, v176
	v_pk_mul_f32 v[2:3], v[182:183], v[2:3]
	v_pk_fma_f32 v[182:183], v[134:135], v[32:33], v[24:25] op_sel_hi:[1,0,1]
	v_pk_fma_f32 v[2:3], v[180:181], v[2:3], v[2:3]
	v_min_f32_e32 v182, 0x40e00000, v182
	v_min_f32_e32 v183, 0x40e00000, v183
	v_cvt_pk_fp8_f32 v197, v2, v3 op_sel:[0,0,1]
	v_pk_mul_f32 v[184:185], v[182:183], s[20:21] op_sel_hi:[1,0]
	v_exp_f32_e32 v184, v184
	v_exp_f32_e32 v185, v185
	s_mov_b32 s28, 0x8000
	v_lshl_add_u64 v[180:181], v[188:189], 0, s[28:29]
	global_store_dwordx2 v[180:181], v[196:197], off
	v_pk_add_f32 v[2:3], v[184:185], 1.0 op_sel_hi:[1,0]
	v_pk_fma_f32 v[180:181], v[102:103], v[32:33], v[16:17] op_sel_hi:[1,0,1]
	v_rcp_f32_e32 v2, v2
	v_rcp_f32_e32 v3, v3
	v_med3_f32 v180, v180, s37, v176
	v_med3_f32 v181, v181, s37, v176
	v_pk_mul_f32 v[2:3], v[182:183], v[2:3]
	v_pk_fma_f32 v[182:183], v[136:137], v[32:33], v[14:15] op_sel_hi:[1,0,1]
	v_pk_fma_f32 v[2:3], v[180:181], v[2:3], v[2:3]
	v_min_f32_e32 v182, 0x40e00000, v182
	v_min_f32_e32 v183, 0x40e00000, v183
	v_pk_mul_f32 v[184:185], v[182:183], s[20:21] op_sel_hi:[1,0]
	v_cvt_pk_fp8_f32 v198, v2, v3
	v_exp_f32_e32 v184, v184
	v_exp_f32_e32 v185, v185
	v_pk_fma_f32 v[180:181], v[104:105], v[32:33], v[12:13] op_sel_hi:[1,0,1]
	v_med3_f32 v180, v180, s37, v176
	v_pk_add_f32 v[2:3], v[184:185], 1.0 op_sel_hi:[1,0]
	v_med3_f32 v181, v181, s37, v176
	v_rcp_f32_e32 v2, v2
	v_rcp_f32_e32 v3, v3
	s_nop 0
	v_pk_mul_f32 v[2:3], v[182:183], v[2:3]
	v_pk_fma_f32 v[182:183], v[130:131], v[32:33], v[10:11] op_sel_hi:[1,0,1]
	v_pk_fma_f32 v[2:3], v[180:181], v[2:3], v[2:3]
	v_min_f32_e32 v182, 0x40e00000, v182
	v_min_f32_e32 v183, 0x40e00000, v183
	v_pk_mul_f32 v[184:185], v[182:183], s[20:21] op_sel_hi:[1,0]
	v_cvt_pk_fp8_f32 v198, v2, v3 op_sel:[0,0,1]
	v_exp_f32_e32 v184, v184
	v_exp_f32_e32 v185, v185
	v_pk_fma_f32 v[180:181], v[98:99], v[32:33], v[8:9] op_sel_hi:[1,0,1]
	v_pk_add_f32 v[2:3], v[184:185], 1.0 op_sel_hi:[1,0]
	s_nop 0
	v_rcp_f32_e32 v2, v2
	v_rcp_f32_e32 v3, v3
	v_med3_f32 v180, v180, s37, v176
	v_med3_f32 v181, v181, s37, v176
	v_pk_mul_f32 v[2:3], v[182:183], v[2:3]
	v_pk_fma_f32 v[182:183], v[132:133], v[32:33], v[6:7] op_sel_hi:[1,0,1]
	v_pk_fma_f32 v[2:3], v[180:181], v[2:3], v[2:3]
	v_min_f32_e32 v182, 0x40e00000, v182
	v_min_f32_e32 v183, 0x40e00000, v183
	v_pk_mul_f32 v[184:185], v[182:183], s[20:21] op_sel_hi:[1,0]
	v_cvt_pk_fp8_f32 v199, v2, v3
	v_exp_f32_e32 v184, v184
	v_exp_f32_e32 v185, v185
	v_pk_fma_f32 v[32:33], v[100:101], v[32:33], v[4:5] op_sel_hi:[1,0,1]
	v_pk_fma_f32 v[180:181], v[94:95], v[30:31], v[24:25] op_sel_hi:[1,0,1]
	v_med3_f32 v32, v32, s37, v176
	v_pk_add_f32 v[2:3], v[184:185], 1.0 op_sel_hi:[1,0]
	v_med3_f32 v33, v33, s37, v176
	v_rcp_f32_e32 v2, v2
	v_rcp_f32_e32 v3, v3
	v_min_f32_e32 v180, 0x40e00000, v180
	v_min_f32_e32 v181, 0x40e00000, v181
	v_pk_mul_f32 v[2:3], v[182:183], v[2:3]
	s_nop 0
	v_pk_fma_f32 v[2:3], v[32:33], v[2:3], v[2:3]
	v_cvt_pk_fp8_f32 v199, v2, v3 op_sel:[0,0,1]
	v_pk_mul_f32 v[182:183], v[180:181], s[20:21] op_sel_hi:[1,0]
	v_exp_f32_e32 v182, v182
	v_exp_f32_e32 v183, v183
	s_mov_b32 s28, 0xc000
	v_lshl_add_u64 v[32:33], v[188:189], 0, s[28:29]
	global_store_dwordx2 v[32:33], v[198:199], off
	v_pk_add_f32 v[32:33], v[182:183], 1.0 op_sel_hi:[1,0]
	v_pk_fma_f32 v[182:183], v[62:63], v[30:31], v[16:17] op_sel_hi:[1,0,1]
	v_rcp_f32_e32 v32, v32
	v_rcp_f32_e32 v33, v33
	v_med3_f32 v182, v182, s37, v176
	v_med3_f32 v183, v183, s37, v176
	v_pk_mul_f32 v[32:33], v[180:181], v[32:33]
	v_pk_fma_f32 v[180:181], v[96:97], v[30:31], v[14:15] op_sel_hi:[1,0,1]
	v_pk_fma_f32 v[32:33], v[182:183], v[32:33], v[32:33]
	v_min_f32_e32 v180, 0x40e00000, v180
	v_min_f32_e32 v181, 0x40e00000, v181
	v_pk_mul_f32 v[184:185], v[180:181], s[20:21] op_sel_hi:[1,0]
	v_cvt_pk_fp8_f32 v200, v32, v33
	v_exp_f32_e32 v184, v184
	v_exp_f32_e32 v185, v185
	v_pk_fma_f32 v[182:183], v[64:65], v[30:31], v[12:13] op_sel_hi:[1,0,1]
	v_med3_f32 v182, v182, s37, v176
	v_pk_add_f32 v[32:33], v[184:185], 1.0 op_sel_hi:[1,0]
	v_med3_f32 v183, v183, s37, v176
	v_rcp_f32_e32 v32, v32
	v_rcp_f32_e32 v33, v33
	s_nop 0
	v_pk_mul_f32 v[32:33], v[180:181], v[32:33]
	v_pk_fma_f32 v[180:181], v[90:91], v[30:31], v[10:11] op_sel_hi:[1,0,1]
	v_pk_fma_f32 v[32:33], v[182:183], v[32:33], v[32:33]
	v_min_f32_e32 v180, 0x40e00000, v180
	v_min_f32_e32 v181, 0x40e00000, v181
	v_pk_mul_f32 v[184:185], v[180:181], s[20:21] op_sel_hi:[1,0]
	v_cvt_pk_fp8_f32 v200, v32, v33 op_sel:[0,0,1]
	v_exp_f32_e32 v184, v184
	v_exp_f32_e32 v185, v185
	v_pk_fma_f32 v[182:183], v[58:59], v[30:31], v[8:9] op_sel_hi:[1,0,1]
	v_med3_f32 v182, v182, s37, v176
	v_pk_add_f32 v[32:33], v[184:185], 1.0 op_sel_hi:[1,0]
	v_med3_f32 v183, v183, s37, v176
	v_rcp_f32_e32 v32, v32
	v_rcp_f32_e32 v33, v33
	s_nop 0
	v_pk_mul_f32 v[32:33], v[180:181], v[32:33]
	v_pk_fma_f32 v[180:181], v[92:93], v[30:31], v[6:7] op_sel_hi:[1,0,1]
	v_pk_fma_f32 v[32:33], v[182:183], v[32:33], v[32:33]
	v_min_f32_e32 v180, 0x40e00000, v180
	v_min_f32_e32 v181, 0x40e00000, v181
	v_pk_mul_f32 v[184:185], v[180:181], s[20:21] op_sel_hi:[1,0]
	v_cvt_pk_fp8_f32 v201, v32, v33
	v_exp_f32_e32 v184, v184
	v_exp_f32_e32 v185, v185
	v_pk_fma_f32 v[30:31], v[60:61], v[30:31], v[4:5] op_sel_hi:[1,0,1]
	v_med3_f32 v30, v30, s37, v176
	v_pk_add_f32 v[32:33], v[184:185], 1.0 op_sel_hi:[1,0]
	v_med3_f32 v31, v31, s37, v176
	v_rcp_f32_e32 v32, v32
	v_rcp_f32_e32 v33, v33
	s_nop 0
	v_pk_mul_f32 v[32:33], v[180:181], v[32:33]
	s_nop 0
	v_pk_fma_f32 v[30:31], v[30:31], v[32:33], v[32:33]
	v_pk_fma_f32 v[32:33], v[86:87], v[28:29], v[24:25] op_sel_hi:[1,0,1]
	v_cvt_pk_fp8_f32 v201, v30, v31 op_sel:[0,0,1]
	v_min_f32_e32 v32, 0x40e00000, v32
	v_min_f32_e32 v33, 0x40e00000, v33
	v_pk_mul_f32 v[180:181], v[32:33], s[20:21] op_sel_hi:[1,0]
	v_exp_f32_e32 v180, v180
	v_exp_f32_e32 v181, v181
	s_mov_b32 s28, 0x20000
	v_lshl_add_u64 v[2:3], v[188:189], 0, s[28:29]
	global_store_dwordx2 v[2:3], v[200:201], off
	v_pk_add_f32 v[2:3], v[180:181], 1.0 op_sel_hi:[1,0]
	v_pk_fma_f32 v[30:31], v[54:55], v[28:29], v[16:17] op_sel_hi:[1,0,1]
	v_rcp_f32_e32 v2, v2
	v_rcp_f32_e32 v3, v3
	v_med3_f32 v30, v30, s37, v176
	v_med3_f32 v31, v31, s37, v176
	v_pk_mul_f32 v[2:3], v[32:33], v[2:3]
	v_pk_fma_f32 v[32:33], v[88:89], v[28:29], v[14:15] op_sel_hi:[1,0,1]
	v_pk_fma_f32 v[2:3], v[30:31], v[2:3], v[2:3]
	v_min_f32_e32 v32, 0x40e00000, v32
	v_min_f32_e32 v33, 0x40e00000, v33
	v_pk_mul_f32 v[180:181], v[32:33], s[20:21] op_sel_hi:[1,0]
	v_cvt_pk_fp8_f32 v202, v2, v3
	v_exp_f32_e32 v180, v180
	v_exp_f32_e32 v181, v181
	v_pk_fma_f32 v[30:31], v[56:57], v[28:29], v[12:13] op_sel_hi:[1,0,1]
	v_med3_f32 v30, v30, s37, v176
	v_pk_add_f32 v[2:3], v[180:181], 1.0 op_sel_hi:[1,0]
	v_med3_f32 v31, v31, s37, v176
	v_rcp_f32_e32 v2, v2
	v_rcp_f32_e32 v3, v3
	s_nop 0
	v_pk_mul_f32 v[2:3], v[32:33], v[2:3]
	v_pk_fma_f32 v[32:33], v[82:83], v[28:29], v[10:11] op_sel_hi:[1,0,1]
	v_pk_fma_f32 v[2:3], v[30:31], v[2:3], v[2:3]
	v_min_f32_e32 v32, 0x40e00000, v32
	v_min_f32_e32 v33, 0x40e00000, v33
	v_pk_mul_f32 v[180:181], v[32:33], s[20:21] op_sel_hi:[1,0]
	v_cvt_pk_fp8_f32 v202, v2, v3 op_sel:[0,0,1]
	v_exp_f32_e32 v180, v180
	v_exp_f32_e32 v181, v181
	v_pk_fma_f32 v[30:31], v[50:51], v[28:29], v[8:9] op_sel_hi:[1,0,1]
	v_pk_add_f32 v[2:3], v[180:181], 1.0 op_sel_hi:[1,0]
	s_nop 0
	v_rcp_f32_e32 v2, v2
	v_rcp_f32_e32 v3, v3
	v_med3_f32 v30, v30, s37, v176
	v_med3_f32 v31, v31, s37, v176
	v_pk_mul_f32 v[2:3], v[32:33], v[2:3]
	v_pk_fma_f32 v[32:33], v[84:85], v[28:29], v[6:7] op_sel_hi:[1,0,1]
	v_pk_fma_f32 v[2:3], v[30:31], v[2:3], v[2:3]
	v_min_f32_e32 v32, 0x40e00000, v32
	v_min_f32_e32 v33, 0x40e00000, v33
	v_pk_mul_f32 v[180:181], v[32:33], s[20:21] op_sel_hi:[1,0]
	v_cvt_pk_fp8_f32 v203, v2, v3
	v_exp_f32_e32 v180, v180
	v_exp_f32_e32 v181, v181
	v_pk_fma_f32 v[28:29], v[52:53], v[28:29], v[4:5] op_sel_hi:[1,0,1]
	v_pk_fma_f32 v[30:31], v[78:79], v[26:27], v[24:25] op_sel_hi:[1,0,1]
	v_med3_f32 v28, v28, s37, v176
	v_pk_add_f32 v[2:3], v[180:181], 1.0 op_sel_hi:[1,0]
	v_med3_f32 v29, v29, s37, v176
	v_rcp_f32_e32 v2, v2
	v_rcp_f32_e32 v3, v3
	v_min_f32_e32 v30, 0x40e00000, v30
	v_min_f32_e32 v31, 0x40e00000, v31
	v_pk_mul_f32 v[2:3], v[32:33], v[2:3]
	s_nop 0
	v_pk_fma_f32 v[2:3], v[28:29], v[2:3], v[2:3]
	v_cvt_pk_fp8_f32 v203, v2, v3 op_sel:[0,0,1]
	v_pk_mul_f32 v[32:33], v[30:31], s[20:21] op_sel_hi:[1,0]
	v_exp_f32_e32 v32, v32
	v_exp_f32_e32 v33, v33
	s_mov_b32 s28, 0x24000
	v_lshl_add_u64 v[28:29], v[188:189], 0, s[28:29]
	global_store_dwordx2 v[28:29], v[202:203], off
	v_pk_add_f32 v[2:3], v[32:33], 1.0 op_sel_hi:[1,0]
	v_pk_fma_f32 v[28:29], v[46:47], v[26:27], v[16:17] op_sel_hi:[1,0,1]
	v_rcp_f32_e32 v2, v2
	v_rcp_f32_e32 v3, v3
	v_med3_f32 v28, v28, s37, v176
	v_med3_f32 v29, v29, s37, v176
	v_pk_mul_f32 v[2:3], v[30:31], v[2:3]
	v_pk_fma_f32 v[30:31], v[80:81], v[26:27], v[14:15] op_sel_hi:[1,0,1]
	v_pk_fma_f32 v[2:3], v[28:29], v[2:3], v[2:3]
	v_min_f32_e32 v30, 0x40e00000, v30
	v_min_f32_e32 v31, 0x40e00000, v31
	v_pk_mul_f32 v[32:33], v[30:31], s[20:21] op_sel_hi:[1,0]
	v_cvt_pk_fp8_f32 v204, v2, v3
	v_exp_f32_e32 v32, v32
	v_exp_f32_e32 v33, v33
	v_pk_fma_f32 v[28:29], v[48:49], v[26:27], v[12:13] op_sel_hi:[1,0,1]
	v_med3_f32 v28, v28, s37, v176
	v_pk_add_f32 v[2:3], v[32:33], 1.0 op_sel_hi:[1,0]
	v_med3_f32 v29, v29, s37, v176
	v_rcp_f32_e32 v2, v2
	v_rcp_f32_e32 v3, v3
	s_nop 0
	v_pk_mul_f32 v[2:3], v[30:31], v[2:3]
	v_pk_fma_f32 v[30:31], v[74:75], v[26:27], v[10:11] op_sel_hi:[1,0,1]
	v_pk_fma_f32 v[2:3], v[28:29], v[2:3], v[2:3]
	v_min_f32_e32 v30, 0x40e00000, v30
	v_min_f32_e32 v31, 0x40e00000, v31
	v_pk_mul_f32 v[32:33], v[30:31], s[20:21] op_sel_hi:[1,0]
	v_cvt_pk_fp8_f32 v204, v2, v3 op_sel:[0,0,1]
	v_exp_f32_e32 v32, v32
	v_exp_f32_e32 v33, v33
	v_pk_fma_f32 v[28:29], v[42:43], v[26:27], v[8:9] op_sel_hi:[1,0,1]
	v_pk_fma_f32 v[24:25], v[70:71], v[22:23], v[24:25] op_sel_hi:[1,0,1]
	v_med3_f32 v28, v28, s37, v176
	v_pk_add_f32 v[2:3], v[32:33], 1.0 op_sel_hi:[1,0]
	v_med3_f32 v29, v29, s37, v176
	v_rcp_f32_e32 v2, v2
	v_rcp_f32_e32 v3, v3
	v_min_f32_e32 v24, 0x40e00000, v24
	v_min_f32_e32 v25, 0x40e00000, v25
	v_pk_fma_f32 v[14:15], v[72:73], v[22:23], v[14:15] op_sel_hi:[1,0,1]
	v_pk_mul_f32 v[2:3], v[30:31], v[2:3]
	v_pk_fma_f32 v[30:31], v[76:77], v[26:27], v[6:7] op_sel_hi:[1,0,1]
	v_pk_fma_f32 v[2:3], v[28:29], v[2:3], v[2:3]
	v_min_f32_e32 v30, 0x40e00000, v30
	v_min_f32_e32 v31, 0x40e00000, v31
	v_pk_mul_f32 v[32:33], v[30:31], s[20:21] op_sel_hi:[1,0]
	v_exp_f32_e32 v32, v32
	v_exp_f32_e32 v33, v33
	v_cvt_pk_fp8_f32 v205, v2, v3
	v_pk_fma_f32 v[26:27], v[44:45], v[26:27], v[4:5] op_sel_hi:[1,0,1]
	v_min_f32_e32 v14, 0x40e00000, v14
	v_pk_add_f32 v[2:3], v[32:33], 1.0 op_sel_hi:[1,0]
	v_med3_f32 v26, v26, s37, v176
	v_rcp_f32_e32 v2, v2
	v_rcp_f32_e32 v3, v3
	v_med3_f32 v27, v27, s37, v176
	v_min_f32_e32 v15, 0x40e00000, v15
	v_pk_fma_f32 v[16:17], v[38:39], v[22:23], v[16:17] op_sel_hi:[1,0,1]
	v_pk_mul_f32 v[2:3], v[30:31], v[2:3]
	v_med3_f32 v16, v16, s37, v176
	v_pk_fma_f32 v[2:3], v[26:27], v[2:3], v[2:3]
	v_cvt_pk_fp8_f32 v205, v2, v3 op_sel:[0,0,1]
	v_pk_mul_f32 v[28:29], v[24:25], s[20:21] op_sel_hi:[1,0]
	v_exp_f32_e32 v28, v28
	v_exp_f32_e32 v29, v29
	s_mov_b32 s28, 0x28000
	v_lshl_add_u64 v[26:27], v[188:189], 0, s[28:29]
	global_store_dwordx2 v[26:27], v[204:205], off
	v_pk_add_f32 v[2:3], v[28:29], 1.0 op_sel_hi:[1,0]
	v_med3_f32 v17, v17, s37, v176
	v_rcp_f32_e32 v2, v2
	v_rcp_f32_e32 v3, v3
	v_pk_fma_f32 v[10:11], v[66:67], v[22:23], v[10:11] op_sel_hi:[1,0,1]
	v_pk_fma_f32 v[12:13], v[40:41], v[22:23], v[12:13] op_sel_hi:[1,0,1]
	v_min_f32_e32 v10, 0x40e00000, v10
	v_pk_mul_f32 v[2:3], v[24:25], v[2:3]
	v_pk_mul_f32 v[24:25], v[14:15], s[20:21] op_sel_hi:[1,0]
	v_pk_fma_f32 v[2:3], v[16:17], v[2:3], v[2:3]
	v_exp_f32_e32 v24, v24
	v_exp_f32_e32 v25, v25
	v_cvt_pk_fp8_f32 v206, v2, v3
	v_min_f32_e32 v11, 0x40e00000, v11
	v_pk_add_f32 v[2:3], v[24:25], 1.0 op_sel_hi:[1,0]
	v_med3_f32 v12, v12, s37, v176
	v_rcp_f32_e32 v2, v2
	v_rcp_f32_e32 v3, v3
	v_med3_f32 v13, v13, s37, v176
	v_pk_fma_f32 v[6:7], v[68:69], v[22:23], v[6:7] op_sel_hi:[1,0,1]
	v_pk_fma_f32 v[8:9], v[34:35], v[22:23], v[8:9] op_sel_hi:[1,0,1]
	v_pk_mul_f32 v[2:3], v[14:15], v[2:3]
	v_pk_mul_f32 v[14:15], v[10:11], s[20:21] op_sel_hi:[1,0]
	v_pk_fma_f32 v[2:3], v[12:13], v[2:3], v[2:3]
	v_exp_f32_e32 v14, v14
	v_exp_f32_e32 v15, v15
	v_cvt_pk_fp8_f32 v206, v2, v3 op_sel:[0,0,1]
	v_min_f32_e32 v6, 0x40e00000, v6
	v_pk_add_f32 v[2:3], v[14:15], 1.0 op_sel_hi:[1,0]
	v_min_f32_e32 v7, 0x40e00000, v7
	v_rcp_f32_e32 v2, v2
	v_rcp_f32_e32 v3, v3
	v_med3_f32 v8, v8, s37, v176
	v_med3_f32 v9, v9, s37, v176
	v_pk_fma_f32 v[4:5], v[36:37], v[22:23], v[4:5] op_sel_hi:[1,0,1]
	v_pk_mul_f32 v[2:3], v[10:11], v[2:3]
	v_pk_mul_f32 v[10:11], v[6:7], s[20:21] op_sel_hi:[1,0]
	v_pk_fma_f32 v[2:3], v[8:9], v[2:3], v[2:3]
	v_exp_f32_e32 v10, v10
	v_exp_f32_e32 v11, v11
	v_cvt_pk_fp8_f32 v207, v2, v3
	v_med3_f32 v4, v4, s37, v176
	v_pk_add_f32 v[2:3], v[10:11], 1.0 op_sel_hi:[1,0]
	v_med3_f32 v5, v5, s37, v176
	v_rcp_f32_e32 v2, v2
	v_rcp_f32_e32 v3, v3
	s_nop 0
	v_pk_mul_f32 v[2:3], v[6:7], v[2:3]
	s_nop 0
	v_pk_fma_f32 v[2:3], v[4:5], v[2:3], v[2:3]
	v_cvt_pk_fp8_f32 v207, v2, v3 op_sel:[0,0,1]
	s_mov_b32 s28, 0x2c000
	v_lshl_add_u64 v[4:5], v[188:189], 0, s[28:29]
	global_store_dwordx2 v[4:5], v[206:207], off
	s_setprio 0
	s_cbranch_vccnz .LBB0_1920
	s_andn2_b64 vcc, exec, s[0:1]
	s_cbranch_vccnz .LBB0_1919
	s_barrier

.LBB0_2094:
.LBB0_2096:
	s_cmp_lg_u64 s[12:13], 0
	s_cbranch_scc0 .Lepi7_noprio
	s_setprio 1
.Lepi7_noprio:
	v_mov_b32_e32 v2, v166
	v_mov_b32_e32 v3, v165
	v_mov_b32_e32 v4, s39
	ds_read_b32 v4, v4 offset:288
	s_lshl_b32 s15, s85, 11
	v_lshlrev_b32_e32 v18, 3, v2
	s_add_i32 s15, s15, 0
	s_add_i32 s15, s15, 0x21000
	v_add_u32_e32 v2, s66, v18
	v_lshl_add_u32 v8, v2, 2, s15
	ds_read_b128 v[10:13], v8
	s_waitcnt lgkmcnt(1)
	v_readfirstlane_b32 s17, v4
	s_lshl_b32 s17, s17, 2
	s_add_i32 s17, s17, 0
	s_add_i32 s17, s17, 0x201c0
	v_mov_b32_e32 v2, s17
	ds_read2_b32 v[6:7], v2 offset1:32
	v_add_u32_e32 v19, s29, v3
	v_add_u32_e32 v21, 16, v19
	v_add_u32_e32 v23, 32, v19
	v_lshl_add_u32 v22, v21, 2, s15
	s_waitcnt lgkmcnt(0)
	v_readfirstlane_b32 s17, v7
	s_sub_i32 s17, s22, s17
	v_readfirstlane_b32 s26, v6
	v_lshl_add_u32 v6, v19, 2, s15
	v_lshl_add_u32 v24, v23, 2, s15
	ds_read_b128 v[14:17], v8 offset:16
	ds_read_b128 v[2:5], v8 offset:512
	s_lshl_b32 s17, s17, 8
	ds_read_b32 v25, v6 offset:1024
	ds_read_b128 v[6:9], v8 offset:528
	ds_read_b32 v22, v22 offset:1024
	ds_read_b32 v24, v24 offset:1024
	v_add_u32_e32 v20, s17, v19
	v_cmp_gt_i32_e32 vcc, s26, v20
	v_add_u32_e32 v20, s17, v21
	v_add_u32_e32 v27, 0xa0, v19
	s_waitcnt lgkmcnt(3)
	v_cndmask_b32_e32 v176, 0, v25, vcc
	v_cmp_gt_i32_e32 vcc, s26, v20
	v_add_u32_e32 v20, s17, v23
	v_add_u32_e32 v29, 0xb0, v19
	s_waitcnt lgkmcnt(1)
	v_cndmask_b32_e32 v178, 0, v22, vcc
	v_cmp_gt_i32_e32 vcc, s26, v20
	v_add_u32_e32 v20, 48, v19
	v_add_u32_e32 v22, 0x80, v19
	s_waitcnt lgkmcnt(0)
	v_cndmask_b32_e32 v32, 0, v24, vcc
	v_add_u32_e32 v24, 0x90, v19
	v_lshl_add_u32 v21, v20, 2, s15
	v_add_u32_e32 v20, s17, v20
	v_lshl_add_u32 v23, v22, 2, s15
	v_lshl_add_u32 v25, v24, 2, s15
	v_lshl_add_u32 v26, v27, 2, s15
	v_lshl_add_u32 v28, v29, 2, s15
	ds_read_b32 v21, v21 offset:1024
	ds_read_b32 v23, v23 offset:1024
	ds_read_b32 v25, v25 offset:1024
	ds_read_b32 v31, v26 offset:1024
	ds_read_b32 v33, v28 offset:1024
	v_cmp_gt_i32_e32 vcc, s26, v20
	v_add_u32_e32 v20, s17, v22
	v_mul_f32_e32 v180, 0x3b800000, v176
	s_waitcnt lgkmcnt(4)
	v_cndmask_b32_e32 v30, 0, v21, vcc
	v_cmp_gt_i32_e32 vcc, s26, v20
	v_lshl_add_u32 v22, s22, 8, v19
	v_pk_mul_f32 v[158:159], v[158:159], v[180:181] op_sel_hi:[1,0]
	s_waitcnt lgkmcnt(3)
	v_cndmask_b32_e32 v28, 0, v23, vcc
	v_add_u32_e32 v20, s17, v24
	v_ashrrev_i32_e32 v23, 31, v22
	v_pk_fma_f32 v[158:159], v[10:11], v[176:177], v[158:159] op_sel_hi:[1,0,1]
	v_pk_mul_f32 v[154:155], v[154:155], v[180:181] op_sel_hi:[1,0]
	v_cmp_gt_i32_e32 vcc, s26, v20
	v_lshlrev_b64 v[182:183], 10, v[22:23]
	v_pk_fma_f32 v[154:155], v[14:15], v[176:177], v[154:155] op_sel_hi:[1,0,1]
	v_med3_f32 v21, v158, s83, v173
	v_med3_f32 v23, v159, s83, v173
	v_mov_b32_e32 v158, 0
	s_waitcnt lgkmcnt(2)
	v_cndmask_b32_e32 v26, 0, v25, vcc
	v_add_u32_e32 v20, s17, v27
	v_cvt_pk_fp8_f32 v158, v21, v23
	v_med3_f32 v25, v154, s83, v173
	v_med3_f32 v27, v155, s83, v173
	v_mov_b32_e32 v159, 0
	v_pk_mul_f32 v[160:161], v[160:161], v[180:181] op_sel_hi:[1,0]
	v_cvt_pk_fp8_f32 v159, v25, v27
	v_pk_fma_f32 v[160:161], v[12:13], v[176:177], v[160:161] op_sel_hi:[1,0,1]
	v_pk_mul_f32 v[156:157], v[156:157], v[180:181] op_sel_hi:[1,0]
	v_med3_f32 v21, v160, s83, v173
	v_pk_fma_f32 v[156:157], v[16:17], v[176:177], v[156:157] op_sel_hi:[1,0,1]
	v_med3_f32 v23, v161, s83, v173
	v_pk_mul_f32 v[150:151], v[150:151], v[180:181] op_sel_hi:[1,0]
	v_cvt_pk_fp8_f32 v158, v21, v23 op_sel:[0,0,1]
	v_med3_f32 v21, v156, s83, v173
	v_med3_f32 v23, v157, s83, v173
	v_pk_fma_f32 v[150:151], v[2:3], v[176:177], v[150:151] op_sel_hi:[1,0,1]
	v_pk_mul_f32 v[146:147], v[146:147], v[180:181] op_sel_hi:[1,0]
	v_cvt_pk_fp8_f32 v159, v21, v23 op_sel:[0,0,1]
	v_pk_fma_f32 v[146:147], v[6:7], v[176:177], v[146:147] op_sel_hi:[1,0,1]
	v_med3_f32 v21, v150, s83, v173
	v_med3_f32 v23, v151, s83, v173
	v_mov_b32_e32 v150, 0
	v_cvt_pk_fp8_f32 v150, v21, v23
	v_med3_f32 v25, v146, s83, v173
	v_med3_f32 v27, v147, s83, v173
	v_mov_b32_e32 v151, 0
	v_pk_mul_f32 v[152:153], v[152:153], v[180:181] op_sel_hi:[1,0]
	v_cvt_pk_fp8_f32 v151, v25, v27
	v_pk_fma_f32 v[152:153], v[4:5], v[176:177], v[152:153] op_sel_hi:[1,0,1]
	v_pk_mul_f32 v[148:149], v[148:149], v[180:181] op_sel_hi:[1,0]
	v_med3_f32 v21, v152, s83, v173
	v_pk_fma_f32 v[148:149], v[8:9], v[176:177], v[148:149] op_sel_hi:[1,0,1]
	v_med3_f32 v23, v153, s83, v173
	s_or_b32 s27, s38, s66
	v_cvt_pk_fp8_f32 v150, v21, v23 op_sel:[0,0,1]
	v_med3_f32 v21, v148, s83, v173
	v_med3_f32 v23, v149, s83, v173
	v_add_u32_e32 v18, s27, v18
	v_cvt_pk_fp8_f32 v151, v21, v23 op_sel:[0,0,1]
	v_ashrrev_i32_e32 v19, 31, v18
	v_lshl_add_u64 v[146:147], s[10:11], 0, v[182:183]
	v_lshl_add_u64 v[146:147], v[146:147], 0, v[18:19]
	global_store_dwordx2 v[146:147], v[158:159], off
	global_store_dwordx2 v[146:147], v[150:151], off offset:128
	v_mul_f32_e32 v146, 0x3b800000, v178
	v_pk_mul_f32 v[142:143], v[142:143], v[146:147] op_sel_hi:[1,0]
	v_pk_mul_f32 v[138:139], v[138:139], v[146:147] op_sel_hi:[1,0]
	v_pk_fma_f32 v[142:143], v[10:11], v[178:179], v[142:143] op_sel_hi:[1,0,1]
	v_pk_fma_f32 v[138:139], v[14:15], v[178:179], v[138:139] op_sel_hi:[1,0,1]
	v_med3_f32 v21, v142, s83, v173
	v_med3_f32 v23, v143, s83, v173
	v_mov_b32_e32 v142, 0
	v_cvt_pk_fp8_f32 v142, v21, v23
	v_med3_f32 v25, v138, s83, v173
	v_med3_f32 v27, v139, s83, v173
	v_mov_b32_e32 v143, 0
	v_pk_mul_f32 v[144:145], v[144:145], v[146:147] op_sel_hi:[1,0]
	v_cvt_pk_fp8_f32 v143, v25, v27
	v_pk_fma_f32 v[144:145], v[12:13], v[178:179], v[144:145] op_sel_hi:[1,0,1]
	v_pk_mul_f32 v[140:141], v[140:141], v[146:147] op_sel_hi:[1,0]
	v_med3_f32 v21, v144, s83, v173
	v_pk_fma_f32 v[140:141], v[16:17], v[178:179], v[140:141] op_sel_hi:[1,0,1]
	v_med3_f32 v23, v145, s83, v173
	v_pk_mul_f32 v[134:135], v[134:135], v[146:147] op_sel_hi:[1,0]
	v_cvt_pk_fp8_f32 v142, v21, v23 op_sel:[0,0,1]
	v_med3_f32 v21, v140, s83, v173
	v_med3_f32 v23, v141, s83, v173
	v_pk_fma_f32 v[134:135], v[2:3], v[178:179], v[134:135] op_sel_hi:[1,0,1]
	v_pk_mul_f32 v[130:131], v[130:131], v[146:147] op_sel_hi:[1,0]
	v_cvt_pk_fp8_f32 v143, v21, v23 op_sel:[0,0,1]
	v_pk_fma_f32 v[130:131], v[6:7], v[178:179], v[130:131] op_sel_hi:[1,0,1]
	v_med3_f32 v21, v134, s83, v173
	v_med3_f32 v23, v135, s83, v173
	v_mov_b32_e32 v134, 0
	v_cvt_pk_fp8_f32 v134, v21, v23
	v_med3_f32 v25, v130, s83, v173
	v_med3_f32 v27, v131, s83, v173
	v_mov_b32_e32 v135, 0
	v_pk_mul_f32 v[136:137], v[136:137], v[146:147] op_sel_hi:[1,0]
	v_cvt_pk_fp8_f32 v135, v25, v27
	v_pk_fma_f32 v[136:137], v[4:5], v[178:179], v[136:137] op_sel_hi:[1,0,1]
	v_pk_mul_f32 v[132:133], v[132:133], v[146:147] op_sel_hi:[1,0]
	v_add_u32_e32 v148, 16, v22
	v_pk_fma_f32 v[132:133], v[8:9], v[178:179], v[132:133] op_sel_hi:[1,0,1]
	v_med3_f32 v21, v136, s83, v173
	v_med3_f32 v23, v137, s83, v173
	v_ashrrev_i32_e32 v149, 31, v148
	v_cvt_pk_fp8_f32 v134, v21, v23 op_sel:[0,0,1]
	v_med3_f32 v21, v132, s83, v173
	v_med3_f32 v23, v133, s83, v173
	v_lshlrev_b64 v[148:149], 10, v[148:149]
	v_cvt_pk_fp8_f32 v135, v21, v23 op_sel:[0,0,1]
	v_lshl_add_u64 v[130:131], s[10:11], 0, v[148:149]
	v_lshl_add_u64 v[130:131], v[130:131], 0, v[18:19]
	global_store_dwordx2 v[130:131], v[142:143], off
	global_store_dwordx2 v[130:131], v[134:135], off offset:128
	v_mul_f32_e32 v130, 0x3b800000, v32
	v_pk_mul_f32 v[126:127], v[126:127], v[130:131] op_sel_hi:[1,0]
	v_pk_mul_f32 v[122:123], v[122:123], v[130:131] op_sel_hi:[1,0]
	s_waitcnt lgkmcnt(0)
	v_pk_fma_f32 v[126:127], v[10:11], v[32:33], v[126:127] op_sel_hi:[1,0,1]
	v_pk_fma_f32 v[122:123], v[14:15], v[32:33], v[122:123] op_sel_hi:[1,0,1]
	v_med3_f32 v21, v126, s83, v173
	v_med3_f32 v23, v127, s83, v173
	v_mov_b32_e32 v126, 0
	v_cvt_pk_fp8_f32 v126, v21, v23
	v_med3_f32 v25, v122, s83, v173
	v_med3_f32 v27, v123, s83, v173
	v_mov_b32_e32 v127, 0
	v_pk_mul_f32 v[128:129], v[128:129], v[130:131] op_sel_hi:[1,0]
	v_cvt_pk_fp8_f32 v127, v25, v27
	v_pk_fma_f32 v[128:129], v[12:13], v[32:33], v[128:129] op_sel_hi:[1,0,1]
	v_pk_mul_f32 v[124:125], v[124:125], v[130:131] op_sel_hi:[1,0]
	v_cmp_gt_i32_e32 vcc, s26, v20
	v_add_u32_e32 v20, s17, v29
	v_pk_fma_f32 v[124:125], v[16:17], v[32:33], v[124:125] op_sel_hi:[1,0,1]
	v_med3_f32 v21, v128, s83, v173
	v_med3_f32 v23, v129, s83, v173
	v_pk_mul_f32 v[118:119], v[118:119], v[130:131] op_sel_hi:[1,0]
	v_cndmask_b32_e32 v24, 0, v31, vcc
	v_cmp_gt_i32_e32 vcc, s26, v20
	v_cvt_pk_fp8_f32 v126, v21, v23 op_sel:[0,0,1]
	v_med3_f32 v21, v124, s83, v173
	v_med3_f32 v23, v125, s83, v173
	v_pk_mul_f32 v[120:121], v[120:121], v[130:131] op_sel_hi:[1,0]
	v_pk_fma_f32 v[118:119], v[2:3], v[32:33], v[118:119] op_sel_hi:[1,0,1]
	v_pk_mul_f32 v[114:115], v[114:115], v[130:131] op_sel_hi:[1,0]
	v_pk_mul_f32 v[116:117], v[116:117], v[130:131] op_sel_hi:[1,0]
	v_cndmask_b32_e32 v20, 0, v33, vcc
	v_cvt_pk_fp8_f32 v127, v21, v23 op_sel:[0,0,1]
	v_pk_fma_f32 v[120:121], v[4:5], v[32:33], v[120:121] op_sel_hi:[1,0,1]
	v_pk_fma_f32 v[116:117], v[8:9], v[32:33], v[116:117] op_sel_hi:[1,0,1]
	v_pk_fma_f32 v[32:33], v[6:7], v[32:33], v[114:115] op_sel_hi:[1,0,1]
	v_med3_f32 v21, v118, s83, v173
	v_med3_f32 v23, v119, s83, v173
	v_mov_b32_e32 v114, 0
	v_cvt_pk_fp8_f32 v114, v21, v23
	v_med3_f32 v25, v32, s83, v173
	v_med3_f32 v27, v33, s83, v173
	v_mov_b32_e32 v115, 0
	v_cvt_pk_fp8_f32 v115, v25, v27
	v_add_u32_e32 v132, 32, v22
	v_med3_f32 v21, v120, s83, v173
	v_med3_f32 v23, v121, s83, v173
	v_ashrrev_i32_e32 v133, 31, v132
	v_cvt_pk_fp8_f32 v114, v21, v23 op_sel:[0,0,1]
	v_med3_f32 v21, v116, s83, v173
	v_med3_f32 v23, v117, s83, v173
	v_lshlrev_b64 v[132:133], 10, v[132:133]
	v_cvt_pk_fp8_f32 v115, v21, v23 op_sel:[0,0,1]
	v_lshl_add_u64 v[32:33], s[10:11], 0, v[132:133]
	v_lshl_add_u64 v[32:33], v[32:33], 0, v[18:19]
	global_store_dwordx2 v[32:33], v[126:127], off
	global_store_dwordx2 v[32:33], v[114:115], off offset:128
	v_mul_f32_e32 v32, 0x3b800000, v30
	v_pk_mul_f32 v[110:111], v[110:111], v[32:33] op_sel_hi:[1,0]
	v_pk_mul_f32 v[106:107], v[106:107], v[32:33] op_sel_hi:[1,0]
	v_pk_fma_f32 v[110:111], v[10:11], v[30:31], v[110:111] op_sel_hi:[1,0,1]
	v_pk_fma_f32 v[106:107], v[14:15], v[30:31], v[106:107] op_sel_hi:[1,0,1]
	v_med3_f32 v21, v110, s83, v173
	v_med3_f32 v23, v111, s83, v173
	v_mov_b32_e32 v110, 0
	v_cvt_pk_fp8_f32 v110, v21, v23
	v_med3_f32 v25, v106, s83, v173
	v_med3_f32 v27, v107, s83, v173
	v_mov_b32_e32 v111, 0
	v_pk_mul_f32 v[112:113], v[112:113], v[32:33] op_sel_hi:[1,0]
	v_cvt_pk_fp8_f32 v111, v25, v27
	v_pk_fma_f32 v[112:113], v[12:13], v[30:31], v[112:113] op_sel_hi:[1,0,1]
	v_pk_mul_f32 v[108:109], v[108:109], v[32:33] op_sel_hi:[1,0]
	v_med3_f32 v21, v112, s83, v173
	v_pk_fma_f32 v[108:109], v[16:17], v[30:31], v[108:109] op_sel_hi:[1,0,1]
	v_med3_f32 v23, v113, s83, v173
	v_pk_mul_f32 v[102:103], v[102:103], v[32:33] op_sel_hi:[1,0]
	v_cvt_pk_fp8_f32 v110, v21, v23 op_sel:[0,0,1]
	v_med3_f32 v21, v108, s83, v173
	v_med3_f32 v23, v109, s83, v173
	v_pk_mul_f32 v[104:105], v[104:105], v[32:33] op_sel_hi:[1,0]
	v_pk_fma_f32 v[102:103], v[2:3], v[30:31], v[102:103] op_sel_hi:[1,0,1]
	v_pk_mul_f32 v[98:99], v[98:99], v[32:33] op_sel_hi:[1,0]
	v_pk_mul_f32 v[32:33], v[100:101], v[32:33] op_sel_hi:[1,0]
	v_cvt_pk_fp8_f32 v111, v21, v23 op_sel:[0,0,1]
	v_pk_fma_f32 v[104:105], v[4:5], v[30:31], v[104:105] op_sel_hi:[1,0,1]
	v_pk_fma_f32 v[32:33], v[8:9], v[30:31], v[32:33] op_sel_hi:[1,0,1]
	v_pk_fma_f32 v[30:31], v[6:7], v[30:31], v[98:99] op_sel_hi:[1,0,1]
	v_med3_f32 v21, v102, s83, v173
	v_med3_f32 v23, v103, s83, v173
	v_mov_b32_e32 v98, 0
	v_cvt_pk_fp8_f32 v98, v21, v23
	v_med3_f32 v25, v30, s83, v173
	v_med3_f32 v27, v31, s83, v173
	v_mov_b32_e32 v99, 0
	v_med3_f32 v21, v104, s83, v173
	v_med3_f32 v23, v105, s83, v173
	v_cvt_pk_fp8_f32 v99, v25, v27
	v_cvt_pk_fp8_f32 v98, v21, v23 op_sel:[0,0,1]
	v_med3_f32 v21, v32, s83, v173
	v_mul_f32_e32 v32, 0x3b800000, v28
	v_pk_mul_f32 v[94:95], v[94:95], v[32:33] op_sel_hi:[1,0]
	v_med3_f32 v23, v33, s83, v173
	v_pk_fma_f32 v[94:95], v[10:11], v[28:29], v[94:95] op_sel_hi:[1,0,1]
	v_pk_mul_f32 v[90:91], v[90:91], v[32:33] op_sel_hi:[1,0]
	v_cvt_pk_fp8_f32 v99, v21, v23 op_sel:[0,0,1]
	v_pk_fma_f32 v[90:91], v[14:15], v[28:29], v[90:91] op_sel_hi:[1,0,1]
	v_med3_f32 v21, v94, s83, v173
	v_med3_f32 v23, v95, s83, v173
	v_mov_b32_e32 v94, 0
	v_cvt_pk_fp8_f32 v94, v21, v23
	v_med3_f32 v25, v90, s83, v173
	v_med3_f32 v27, v91, s83, v173
	v_mov_b32_e32 v95, 0
	v_pk_mul_f32 v[96:97], v[96:97], v[32:33] op_sel_hi:[1,0]
	v_cvt_pk_fp8_f32 v95, v25, v27
	v_pk_fma_f32 v[96:97], v[12:13], v[28:29], v[96:97] op_sel_hi:[1,0,1]
	v_pk_mul_f32 v[92:93], v[92:93], v[32:33] op_sel_hi:[1,0]
	v_med3_f32 v21, v96, s83, v173
	v_pk_fma_f32 v[92:93], v[16:17], v[28:29], v[92:93] op_sel_hi:[1,0,1]
	v_med3_f32 v23, v97, s83, v173
	v_pk_mul_f32 v[86:87], v[86:87], v[32:33] op_sel_hi:[1,0]
	v_add_u32_e32 v114, 48, v22
	v_cvt_pk_fp8_f32 v94, v21, v23 op_sel:[0,0,1]
	v_med3_f32 v21, v92, s83, v173
	v_med3_f32 v23, v93, s83, v173
	v_pk_mul_f32 v[88:89], v[88:89], v[32:33] op_sel_hi:[1,0]
	v_pk_fma_f32 v[86:87], v[2:3], v[28:29], v[86:87] op_sel_hi:[1,0,1]
	v_pk_mul_f32 v[82:83], v[82:83], v[32:33] op_sel_hi:[1,0]
	v_pk_mul_f32 v[32:33], v[84:85], v[32:33] op_sel_hi:[1,0]
	v_ashrrev_i32_e32 v115, 31, v114
	v_cvt_pk_fp8_f32 v95, v21, v23 op_sel:[0,0,1]
	v_pk_fma_f32 v[88:89], v[4:5], v[28:29], v[88:89] op_sel_hi:[1,0,1]
	v_pk_fma_f32 v[32:33], v[8:9], v[28:29], v[32:33] op_sel_hi:[1,0,1]
	v_pk_fma_f32 v[28:29], v[6:7], v[28:29], v[82:83] op_sel_hi:[1,0,1]
	v_med3_f32 v21, v86, s83, v173
	v_med3_f32 v23, v87, s83, v173
	v_mov_b32_e32 v82, 0
	v_lshlrev_b64 v[114:115], 10, v[114:115]
	v_cvt_pk_fp8_f32 v82, v21, v23
	v_med3_f32 v25, v28, s83, v173
	v_med3_f32 v27, v29, s83, v173
	v_mov_b32_e32 v83, 0
	v_lshl_add_u64 v[30:31], s[10:11], 0, v[114:115]
	v_cvt_pk_fp8_f32 v83, v25, v27
	v_lshl_add_u64 v[30:31], v[30:31], 0, v[18:19]
	global_store_dwordx2 v[30:31], v[110:111], off
	global_store_dwordx2 v[30:31], v[98:99], off offset:128
	v_add_u32_e32 v30, 0x80, v22
	v_med3_f32 v21, v88, s83, v173
	v_med3_f32 v23, v89, s83, v173
	v_ashrrev_i32_e32 v31, 31, v30
	v_cvt_pk_fp8_f32 v82, v21, v23 op_sel:[0,0,1]
	v_med3_f32 v21, v32, s83, v173
	v_med3_f32 v23, v33, s83, v173
	v_lshlrev_b64 v[30:31], 10, v[30:31]
	v_cvt_pk_fp8_f32 v83, v21, v23 op_sel:[0,0,1]
	v_lshl_add_u64 v[28:29], s[10:11], 0, v[30:31]
	v_lshl_add_u64 v[28:29], v[28:29], 0, v[18:19]
	global_store_dwordx2 v[28:29], v[94:95], off
	global_store_dwordx2 v[28:29], v[82:83], off offset:128
	v_mul_f32_e32 v28, 0x3b800000, v26
	v_pk_mul_f32 v[32:33], v[78:79], v[28:29] op_sel_hi:[1,0]
	v_pk_mul_f32 v[74:75], v[74:75], v[28:29] op_sel_hi:[1,0]
	v_pk_fma_f32 v[32:33], v[10:11], v[26:27], v[32:33] op_sel_hi:[1,0,1]
	v_pk_mul_f32 v[78:79], v[80:81], v[28:29] op_sel_hi:[1,0]
	v_pk_mul_f32 v[76:77], v[76:77], v[28:29] op_sel_hi:[1,0]
	v_pk_fma_f32 v[74:75], v[14:15], v[26:27], v[74:75] op_sel_hi:[1,0,1]
	v_med3_f32 v21, v32, s83, v173
	v_med3_f32 v23, v33, s83, v173
	v_mov_b32_e32 v32, 0
	v_pk_fma_f32 v[78:79], v[12:13], v[26:27], v[78:79] op_sel_hi:[1,0,1]
	v_pk_fma_f32 v[76:77], v[16:17], v[26:27], v[76:77] op_sel_hi:[1,0,1]
	v_cvt_pk_fp8_f32 v32, v21, v23
	v_med3_f32 v25, v74, s83, v173
	v_med3_f32 v27, v75, s83, v173
	v_mov_b32_e32 v33, 0
	v_cvt_pk_fp8_f32 v33, v25, v27
	v_med3_f32 v21, v78, s83, v173
	v_med3_f32 v23, v79, s83, v173
	v_pk_mul_f32 v[70:71], v[70:71], v[28:29] op_sel_hi:[1,0]
	v_cvt_pk_fp8_f32 v32, v21, v23 op_sel:[0,0,1]
	v_med3_f32 v21, v76, s83, v173
	v_med3_f32 v23, v77, s83, v173
	v_pk_mul_f32 v[72:73], v[72:73], v[28:29] op_sel_hi:[1,0]
	v_pk_fma_f32 v[70:71], v[2:3], v[26:27], v[70:71] op_sel_hi:[1,0,1]
	v_pk_mul_f32 v[66:67], v[66:67], v[28:29] op_sel_hi:[1,0]
	v_pk_mul_f32 v[28:29], v[68:69], v[28:29] op_sel_hi:[1,0]
	v_cvt_pk_fp8_f32 v33, v21, v23 op_sel:[0,0,1]
	v_pk_fma_f32 v[72:73], v[4:5], v[26:27], v[72:73] op_sel_hi:[1,0,1]
	v_pk_fma_f32 v[28:29], v[8:9], v[26:27], v[28:29] op_sel_hi:[1,0,1]
	v_pk_fma_f32 v[26:27], v[6:7], v[26:27], v[66:67] op_sel_hi:[1,0,1]
	v_med3_f32 v21, v70, s83, v173
	v_med3_f32 v23, v71, s83, v173
	v_mov_b32_e32 v66, 0
	v_cvt_pk_fp8_f32 v66, v21, v23
	v_med3_f32 v25, v26, s83, v173
	v_med3_f32 v26, v27, s83, v173
	v_mov_b32_e32 v67, 0
	v_cvt_pk_fp8_f32 v67, v25, v26
	v_add_u32_e32 v30, 0x90, v22
	v_med3_f32 v21, v72, s83, v173
	v_med3_f32 v23, v73, s83, v173
	v_ashrrev_i32_e32 v31, 31, v30
	v_cvt_pk_fp8_f32 v66, v21, v23 op_sel:[0,0,1]
	v_med3_f32 v21, v28, s83, v173
	v_med3_f32 v23, v29, s83, v173
	v_lshlrev_b64 v[30:31], 10, v[30:31]
	v_cvt_pk_fp8_f32 v67, v21, v23 op_sel:[0,0,1]
	v_lshl_add_u64 v[26:27], s[10:11], 0, v[30:31]
	v_lshl_add_u64 v[26:27], v[26:27], 0, v[18:19]
	global_store_dwordx2 v[26:27], v[32:33], off
	global_store_dwordx2 v[26:27], v[66:67], off offset:128
	v_mul_f32_e32 v26, 0x3b800000, v24
	v_pk_mul_f32 v[30:31], v[62:63], v[26:27] op_sel_hi:[1,0]
	v_pk_mul_f32 v[58:59], v[58:59], v[26:27] op_sel_hi:[1,0]
	v_pk_fma_f32 v[30:31], v[10:11], v[24:25], v[30:31] op_sel_hi:[1,0,1]
	v_pk_mul_f32 v[32:33], v[64:65], v[26:27] op_sel_hi:[1,0]
	v_pk_mul_f32 v[60:61], v[60:61], v[26:27] op_sel_hi:[1,0]
	v_pk_fma_f32 v[58:59], v[14:15], v[24:25], v[58:59] op_sel_hi:[1,0,1]
	v_med3_f32 v21, v30, s83, v173
	v_med3_f32 v23, v31, s83, v173
	v_mov_b32_e32 v30, 0
	v_pk_fma_f32 v[32:33], v[12:13], v[24:25], v[32:33] op_sel_hi:[1,0,1]
	v_pk_fma_f32 v[60:61], v[16:17], v[24:25], v[60:61] op_sel_hi:[1,0,1]
	v_cvt_pk_fp8_f32 v30, v21, v23
	v_med3_f32 v25, v58, s83, v173
	v_med3_f32 v27, v59, s83, v173
	v_mov_b32_e32 v31, 0
	v_cvt_pk_fp8_f32 v31, v25, v27
	v_med3_f32 v21, v32, s83, v173
	v_med3_f32 v23, v33, s83, v173
	v_pk_mul_f32 v[32:33], v[54:55], v[26:27] op_sel_hi:[1,0]
	v_cvt_pk_fp8_f32 v30, v21, v23 op_sel:[0,0,1]
	v_med3_f32 v21, v60, s83, v173
	v_med3_f32 v23, v61, s83, v173
	v_pk_mul_f32 v[54:55], v[56:57], v[26:27] op_sel_hi:[1,0]
	v_pk_fma_f32 v[32:33], v[2:3], v[24:25], v[32:33] op_sel_hi:[1,0,1]
	v_pk_mul_f32 v[50:51], v[50:51], v[26:27] op_sel_hi:[1,0]
	v_pk_mul_f32 v[26:27], v[52:53], v[26:27] op_sel_hi:[1,0]
	v_cvt_pk_fp8_f32 v31, v21, v23 op_sel:[0,0,1]
	v_pk_fma_f32 v[54:55], v[4:5], v[24:25], v[54:55] op_sel_hi:[1,0,1]
	v_pk_fma_f32 v[26:27], v[8:9], v[24:25], v[26:27] op_sel_hi:[1,0,1]
	v_pk_fma_f32 v[24:25], v[6:7], v[24:25], v[50:51] op_sel_hi:[1,0,1]
	v_med3_f32 v21, v32, s83, v173
	v_med3_f32 v23, v33, s83, v173
	v_mov_b32_e32 v32, 0
	v_cvt_pk_fp8_f32 v32, v21, v23
	v_med3_f32 v24, v24, s83, v173
	v_med3_f32 v25, v25, s83, v173
	v_mov_b32_e32 v33, 0
	v_cvt_pk_fp8_f32 v33, v24, v25
	v_add_u32_e32 v28, 0xa0, v22
	v_med3_f32 v21, v54, s83, v173
	v_med3_f32 v23, v55, s83, v173
	v_ashrrev_i32_e32 v29, 31, v28
	v_cvt_pk_fp8_f32 v32, v21, v23 op_sel:[0,0,1]
	v_med3_f32 v21, v26, s83, v173
	v_med3_f32 v23, v27, s83, v173
	v_lshlrev_b64 v[28:29], 10, v[28:29]
	v_cvt_pk_fp8_f32 v33, v21, v23 op_sel:[0,0,1]
	v_lshl_add_u64 v[24:25], s[10:11], 0, v[28:29]
	v_lshl_add_u64 v[24:25], v[24:25], 0, v[18:19]
	global_store_dwordx2 v[24:25], v[30:31], off
	global_store_dwordx2 v[24:25], v[32:33], off offset:128
	v_mul_f32_e32 v24, 0x3b800000, v20
	v_pk_mul_f32 v[26:27], v[46:47], v[24:25] op_sel_hi:[1,0]
	v_pk_mul_f32 v[28:29], v[48:49], v[24:25] op_sel_hi:[1,0]
	v_pk_fma_f32 v[10:11], v[10:11], v[20:21], v[26:27] op_sel_hi:[1,0,1]
	v_pk_fma_f32 v[12:13], v[12:13], v[20:21], v[28:29] op_sel_hi:[1,0,1]
	v_pk_mul_f32 v[26:27], v[42:43], v[24:25] op_sel_hi:[1,0]
	v_pk_mul_f32 v[28:29], v[44:45], v[24:25] op_sel_hi:[1,0]
	v_pk_fma_f32 v[14:15], v[14:15], v[20:21], v[26:27] op_sel_hi:[1,0,1]
	v_pk_fma_f32 v[16:17], v[16:17], v[20:21], v[28:29] op_sel_hi:[1,0,1]
	v_med3_f32 v21, v10, s83, v173
	v_med3_f32 v11, v11, s83, v173
	v_mov_b32_e32 v10, 0
	v_cvt_pk_fp8_f32 v10, v21, v11
	v_med3_f32 v14, v14, s83, v173
	v_med3_f32 v15, v15, s83, v173
	v_mov_b32_e32 v11, 0
	v_cvt_pk_fp8_f32 v11, v14, v15
	v_med3_f32 v12, v12, s83, v173
	v_med3_f32 v13, v13, s83, v173
	v_cvt_pk_fp8_f32 v10, v12, v13 op_sel:[0,0,1]
	v_med3_f32 v12, v16, s83, v173
	v_med3_f32 v13, v17, s83, v173
	v_cvt_pk_fp8_f32 v11, v12, v13 op_sel:[0,0,1]
	v_pk_mul_f32 v[12:13], v[38:39], v[24:25] op_sel_hi:[1,0]
	v_pk_mul_f32 v[14:15], v[40:41], v[24:25] op_sel_hi:[1,0]
	v_pk_fma_f32 v[2:3], v[2:3], v[20:21], v[12:13] op_sel_hi:[1,0,1]
	v_pk_mul_f32 v[12:13], v[34:35], v[24:25] op_sel_hi:[1,0]
	v_med3_f32 v3, v3, s83, v173
	v_pk_fma_f32 v[6:7], v[6:7], v[20:21], v[12:13] op_sel_hi:[1,0,1]
	v_med3_f32 v12, v2, s83, v173
	v_mov_b32_e32 v2, 0
	v_cvt_pk_fp8_f32 v2, v12, v3
	v_med3_f32 v6, v6, s83, v173
	v_med3_f32 v7, v7, s83, v173
	v_mov_b32_e32 v3, 0
	v_cvt_pk_fp8_f32 v3, v6, v7
	v_pk_fma_f32 v[4:5], v[4:5], v[20:21], v[14:15] op_sel_hi:[1,0,1]
	v_pk_mul_f32 v[14:15], v[36:37], v[24:25] op_sel_hi:[1,0]
	v_add_u32_e32 v22, 0xb0, v22
	v_pk_fma_f32 v[8:9], v[8:9], v[20:21], v[14:15] op_sel_hi:[1,0,1]
	v_med3_f32 v4, v4, s83, v173
	v_med3_f32 v5, v5, s83, v173
	v_ashrrev_i32_e32 v23, 31, v22
	v_cvt_pk_fp8_f32 v2, v4, v5 op_sel:[0,0,1]
	v_med3_f32 v4, v8, s83, v173
	v_med3_f32 v5, v9, s83, v173
	v_lshlrev_b64 v[22:23], 10, v[22:23]
	v_cvt_pk_fp8_f32 v3, v4, v5 op_sel:[0,0,1]
	v_lshl_add_u64 v[4:5], s[10:11], 0, v[22:23]
	v_lshl_add_u64 v[4:5], v[4:5], 0, v[18:19]
	s_and_b64 vcc, exec, s[6:7]
	s_mov_b64 s[6:7], -1
	v_readlane_b32 s90, v253, 26
	global_store_dwordx2 v[4:5], v[10:11], off
	global_store_dwordx2 v[4:5], v[2:3], off offset:128
	s_setprio 0
	s_cbranch_vccnz .LBB0_2057
	s_andn2_b64 vcc, exec, s[8:9]
	s_cbranch_vccnz .LBB0_2056
	s_barrier
	s_branch .LBB0_2056
